# attention: waves 4-7 take the per-tile barrier before their softmax scale/exp section (stagger), waves 0-3 after; on top of LDS-DMA K/V
# baseline (speedup 1.0000x reference)
.LBB0_1344:
	ds_read_b128 v[230:233], v203 offset:24576
	ds_read_b128 v[236:239], v203 offset:36864
	ds_read_b128 v[240:243], v204 offset:24576
	ds_read_b128 v[244:247], v204 offset:36864
	ds_read_b128 v[66:69], v201 offset:36864
	ds_read_b128 v[70:73], v201 offset:24576
	ds_read_b128 v[212:215], v202 offset:24576
	ds_read_b128 v[216:219], v202 offset:36864
	v_add_f32_e32 v168, 0, v169
	v_add_f32_e32 v168, v191, v168
	v_add_f32_e32 v168, v170, v168
	s_waitcnt lgkmcnt(2)
	v_mfma_f32_32x32x16_bf16 v[82:97], v[70:73], v[128:131], 0
	v_add_f32_e32 v168, v192, v168
	v_add_f32_e32 v168, v190, v168
	v_add_f32_e32 v168, v193, v168
	v_add_f32_e32 v168, v171, v168
	v_add_f32_e32 v168, v189, v168
	v_add_f32_e32 v168, v173, v168
	v_add_f32_e32 v168, v175, v168
	v_mfma_f32_32x32x16_bf16 v[66:81], v[66:69], v[128:131], 0
	v_add_f32_e32 v168, v174, v168
	v_add_f32_e32 v168, v188, v168
	v_exp_f32_e32 v162, v162
	v_add_f32_e32 v168, v164, v168
	v_exp_f32_e32 v163, v163
	v_add_f32_e32 v168, v166, v168
	v_exp_f32_e32 v160, v160
	v_mfma_f32_32x32x16_bf16 v[82:97], v[230:233], v[124:127], v[82:97]
	v_add_f32_e32 v168, v165, v168
	v_exp_f32_e32 v161, v161
	v_add_f32_e32 v168, v167, v168
	v_exp_f32_e32 v156, v156
	v_add_f32_e32 v168, v162, v168
	v_exp_f32_e32 v157, v157
	v_add_f32_e32 v168, v163, v168
	v_mfma_f32_32x32x16_bf16 v[66:81], v[236:239], v[124:127], v[66:81]
	ds_read_b128 v[230:233], v201 offset:24704
	ds_read_b128 v[236:239], v201 offset:36992
	v_exp_f32_e32 v152, v152
	v_add_f32_e32 v168, v160, v168
	v_exp_f32_e32 v153, v153
	v_add_f32_e32 v168, v161, v168
	v_exp_f32_e32 v150, v150
	v_add_f32_e32 v168, v156, v168
	v_mfma_f32_32x32x16_bf16 v[82:97], v[240:243], v[120:123], v[82:97]
	v_exp_f32_e32 v151, v151
	v_add_f32_e32 v168, v157, v168
	v_exp_f32_e32 v158, v158
	v_add_f32_e32 v168, v152, v168
	v_exp_f32_e32 v159, v159
	v_add_f32_e32 v168, v153, v168
	v_exp_f32_e32 v154, v154
	v_mfma_f32_32x32x16_bf16 v[66:81], v[244:247], v[120:123], v[66:81]
	ds_read_b128 v[240:243], v203 offset:24704
	ds_read_b128 v[244:247], v203 offset:36992
	v_add_f32_e32 v168, v150, v168
	v_exp_f32_e32 v155, v155
	v_add_f32_e32 v168, v151, v168
	v_exp_f32_e32 v148, v148
	v_add_f32_e32 v168, v158, v168
	v_exp_f32_e32 v149, v149
	s_waitcnt lgkmcnt(5)
	v_mfma_f32_32x32x16_bf16 v[82:97], v[212:215], v[116:119], v[82:97]
	v_add_f32_e32 v168, v159, v168
	v_add_f32_e32 v168, v154, v168
	v_add_f32_e32 v168, v155, v168
	v_add_f32_e32 v168, v148, v168
	s_waitcnt lgkmcnt(4)
	v_mfma_f32_32x32x16_bf16 v[66:81], v[216:219], v[116:119], v[66:81]
	ds_read_b128 v[212:215], v204 offset:24704
	ds_read_b128 v[216:219], v204 offset:36992
	s_waitcnt lgkmcnt(5)
	v_mfma_f32_32x32x16_bf16 v[82:97], v[230:233], v[112:115], v[82:97]
	s_waitcnt lgkmcnt(4)
	v_mfma_f32_32x32x16_bf16 v[66:81], v[236:239], v[112:115], v[66:81]
	ds_read_b128 v[230:233], v202 offset:24704
	ds_read_b128 v[236:239], v202 offset:36992
	s_waitcnt lgkmcnt(5)
	v_mfma_f32_32x32x16_bf16 v[82:97], v[240:243], v[108:111], v[82:97]
	s_waitcnt lgkmcnt(4)
	v_mfma_f32_32x32x16_bf16 v[66:81], v[244:247], v[108:111], v[66:81]
	ds_read_b128 v[240:243], v201 offset:24832
	ds_read_b128 v[244:247], v201 offset:37120
	s_waitcnt lgkmcnt(5)
	v_mfma_f32_32x32x16_bf16 v[82:97], v[212:215], v[104:107], v[82:97]
	s_waitcnt lgkmcnt(4)
	v_mfma_f32_32x32x16_bf16 v[66:81], v[216:219], v[104:107], v[66:81]
	ds_read_b128 v[212:215], v203 offset:24832
	ds_read_b128 v[216:219], v203 offset:37120
	s_waitcnt lgkmcnt(5)
	v_mfma_f32_32x32x16_bf16 v[82:97], v[230:233], v[100:103], v[82:97]
	s_waitcnt lgkmcnt(4)
	v_mfma_f32_32x32x16_bf16 v[66:81], v[236:239], v[100:103], v[66:81]
	ds_read_b128 v[230:233], v204 offset:24832
	ds_read_b128 v[236:239], v204 offset:37120
	s_waitcnt lgkmcnt(5)
	v_mfma_f32_32x32x16_bf16 v[82:97], v[240:243], v[144:147], v[82:97]
	s_waitcnt lgkmcnt(4)
	v_mfma_f32_32x32x16_bf16 v[66:81], v[244:247], v[144:147], v[66:81]
	ds_read_b128 v[240:243], v202 offset:24832
	ds_read_b128 v[244:247], v202 offset:37120
	s_waitcnt lgkmcnt(5)
	v_mfma_f32_32x32x16_bf16 v[82:97], v[212:215], v[140:143], v[82:97]
	v_add_f32_e32 v212, v149, v168
	v_mov_b32_e32 v213, v212
	v_cvt_pk_bf16_f32 v168, v169, v191
	v_cvt_pk_bf16_f32 v169, v170, v192
	v_cvt_pk_bf16_f32 v170, v190, v193
	v_cvt_pk_bf16_f32 v171, v171, v189
	v_cvt_pk_bf16_f32 v172, v173, v175
	s_waitcnt lgkmcnt(4)
	v_mfma_f32_32x32x16_bf16 v[66:81], v[216:219], v[140:143], v[66:81]
	v_cvt_pk_bf16_f32 v173, v174, v188
	v_cvt_pk_bf16_f32 v174, v164, v166
	v_permlane32_swap_b32_e32 v212, v213
	v_permlane32_swap_b32_e32 v168, v170
	v_cvt_pk_bf16_f32 v175, v165, v167
	s_waitcnt lgkmcnt(3)
	v_mfma_f32_32x32x16_bf16 v[82:97], v[230:233], v[136:139], v[82:97]
	v_permlane32_swap_b32_e32 v172, v174
	v_cvt_pk_bf16_f32 v214, v162, v163
	v_cvt_pk_bf16_f32 v215, v160, v161
	v_cvt_pk_bf16_f32 v216, v156, v157
	v_cvt_pk_bf16_f32 v217, v152, v153
	v_cvt_pk_bf16_f32 v230, v150, v151
	s_waitcnt lgkmcnt(2)
	v_mfma_f32_32x32x16_bf16 v[66:81], v[236:239], v[136:139], v[66:81]
	v_cvt_pk_bf16_f32 v231, v158, v159
	v_cvt_pk_bf16_f32 v232, v154, v155
	v_cvt_pk_bf16_f32 v233, v148, v149
	v_permlane32_swap_b32_e32 v169, v171
	v_permlane32_swap_b32_e32 v173, v175
	s_waitcnt lgkmcnt(1)
	v_mfma_f32_32x32x16_bf16 v[82:97], v[240:243], v[132:135], v[82:97]
	v_permlane32_swap_b32_e32 v214, v216
	v_permlane32_swap_b32_e32 v215, v217
	v_permlane32_swap_b32_e32 v230, v232
	v_permlane32_swap_b32_e32 v231, v233
	s_waitcnt lgkmcnt(0)
	v_mfma_f32_32x32x16_bf16 v[66:81], v[244:247], v[132:135], v[66:81]
	v_readfirstlane_b32 s4, v0
	s_nop 0
	s_lshl_b32 s5, s4, 4
	s_mul_i32 s4, s5, 3
	s_add_i32 m0, s4, 0x8000
	s_nop 0
	global_load_lds_dwordx4 v[182:183], off
	s_add_i32 m0, s4, 0x8400
	s_nop 0
	global_load_lds_dwordx4 v[184:185], off
	s_add_i32 m0, s4, 0x8800
	s_nop 0
	global_load_lds_dwordx4 v[186:187], off
	s_lshl_b32 s5, s5, 1
	s_add_i32 m0, s5, 0x4000
	s_nop 0
	global_load_lds_dwordx4 v[206:207], off
	s_add_i32 m0, s5, 0x4380
	s_nop 0
	global_load_lds_dwordx4 v[206:207], off offset:128
	v_add_co_u32_e32 v182, vcc, v182, v205
	s_nop 1
	v_addc_co_u32_e32 v183, vcc, 0, v183, vcc
	v_add_co_u32_e32 v184, vcc, v184, v208
	s_nop 1
	v_addc_co_u32_e32 v185, vcc, 0, v185, vcc
	v_add_co_u32_e32 v186, vcc, v186, v209
	s_nop 1
	v_addc_co_u32_e32 v187, vcc, 0, v187, vcc
	v_add_co_u32_e32 v206, vcc, 0x38000, v206
	s_nop 1
	v_addc_co_u32_e32 v207, vcc, 0, v207, vcc
	ds_read_b64_tr_b16 v[236:237], v200 offset:0
	ds_read_b64_tr_b16 v[238:239], v200 offset:0x800
	ds_read_b64_tr_b16 v[240:241], v200 offset:0x1000
	ds_read_b64_tr_b16 v[242:243], v200 offset:0x1800
	ds_read_b64_tr_b16 v[244:245], v200 offset:0x2000
	ds_read_b64_tr_b16 v[246:247], v200 offset:0x2800
	ds_read_b64_tr_b16 v[222:223], v200 offset:0x3000
	ds_read_b64_tr_b16 v[224:225], v200 offset:0x3800
	s_waitcnt lgkmcnt(0)
	s_nop 0
	v_mfma_f32_32x32x16_bf16 v[2:17], v[168:171], v[236:239], v[2:17]
	v_mfma_f32_32x32x16_bf16 v[2:17], v[172:175], v[240:243], v[2:17]
	v_mfma_f32_32x32x16_bf16 v[2:17], v[214:217], v[244:247], v[2:17]
	v_mfma_f32_32x32x16_bf16 v[2:17], v[230:233], v[222:225], v[2:17]
	ds_read_b64_tr_b16 v[222:223], v200 offset:0x200
	ds_read_b64_tr_b16 v[224:225], v200 offset:0xa00
	ds_read_b64_tr_b16 v[236:237], v200 offset:0x1200
	ds_read_b64_tr_b16 v[238:239], v200 offset:0x1a00
	ds_read_b64_tr_b16 v[240:241], v200 offset:0x2200
	ds_read_b64_tr_b16 v[242:243], v200 offset:0x2a00
	ds_read_b64_tr_b16 v[244:245], v200 offset:0x3200
	ds_read_b64_tr_b16 v[246:247], v200 offset:0x3a00
	s_waitcnt lgkmcnt(0)
	s_nop 0
	v_mfma_f32_32x32x16_bf16 v[50:65], v[168:171], v[222:225], v[50:65]
	ds_read_b64_tr_b16 v[222:223], v200 offset:0x400
	ds_read_b64_tr_b16 v[224:225], v200 offset:0xc00
	v_mfma_f32_32x32x16_bf16 v[50:65], v[172:175], v[236:239], v[50:65]
	ds_read_b64_tr_b16 v[236:237], v200 offset:0x1400
	ds_read_b64_tr_b16 v[238:239], v200 offset:0x1c00
	v_mfma_f32_32x32x16_bf16 v[50:65], v[214:217], v[240:243], v[50:65]
	ds_read_b64_tr_b16 v[240:241], v200 offset:0x2400
	ds_read_b64_tr_b16 v[242:243], v200 offset:0x2c00
	v_mfma_f32_32x32x16_bf16 v[50:65], v[230:233], v[244:247], v[50:65]
	ds_read_b64_tr_b16 v[244:245], v200 offset:0x3400
	ds_read_b64_tr_b16 v[246:247], v200 offset:0x3c00
	s_waitcnt lgkmcnt(0)
	v_mfma_f32_32x32x16_bf16 v[34:49], v[168:171], v[222:225], v[34:49]
	ds_read_b64_tr_b16 v[222:223], v200 offset:0x600
	ds_read_b64_tr_b16 v[224:225], v200 offset:0xe00
	v_mfma_f32_32x32x16_bf16 v[34:49], v[172:175], v[236:239], v[34:49]
	ds_read_b64_tr_b16 v[236:237], v200 offset:0x1600
	ds_read_b64_tr_b16 v[238:239], v200 offset:0x1e00
	v_mfma_f32_32x32x16_bf16 v[34:49], v[214:217], v[240:243], v[34:49]
	ds_read_b64_tr_b16 v[240:241], v200 offset:0x2600
	ds_read_b64_tr_b16 v[242:243], v200 offset:0x2e00
	v_mfma_f32_32x32x16_bf16 v[34:49], v[230:233], v[244:247], v[34:49]
	ds_read_b64_tr_b16 v[244:245], v200 offset:0x3600
	ds_read_b64_tr_b16 v[246:247], v200 offset:0x3e00
	s_waitcnt lgkmcnt(0)
	v_mfma_f32_32x32x16_bf16 v[18:33], v[168:171], v[222:225], v[18:33]
	v_max_f32_e32 v168, v83, v83
	v_max_f32_e32 v169, v82, v82
	v_max_f32_e32 v168, v169, v168
	v_max3_f32 v168, v168, v84, v85
	v_max3_f32 v168, v168, v86, v87
	v_max3_f32 v168, v168, v88, v89
	v_max3_f32 v168, v168, v90, v91
	v_max3_f32 v168, v168, v92, v93
	v_max3_f32 v168, v168, v94, v95
	v_mfma_f32_32x32x16_bf16 v[18:33], v[172:175], v[236:239], v[18:33]
	v_max3_f32 v168, v168, v96, v97
	v_max3_f32 v168, v168, v66, v67
	v_max3_f32 v168, v168, v68, v69
	v_max3_f32 v168, v168, v70, v71
	v_max3_f32 v168, v168, v72, v73
	v_max3_f32 v168, v168, v74, v75
	v_max3_f32 v168, v168, v76, v77
	v_max3_f32 v168, v168, v78, v79
	v_mfma_f32_32x32x16_bf16 v[18:33], v[214:217], v[240:243], v[18:33]
	v_max3_f32 v168, v168, v80, v81
	v_mov_b32_e32 v169, v168
	s_nop 1
	v_permlane32_swap_b32_e32 v168, v169
	v_max_f32_e32 v169, v169, v169
	v_max_f32_e32 v168, v168, v168
	v_max_f32_e32 v168, v168, v169
	v_sub_f32_e32 v169, v168, v211
	v_cmp_ge_f32_e32 vcc, s11, v169
	v_max_f32_e32 v169, v211, v211
	v_max_f32_e32 v168, v169, v168
	v_mfma_f32_32x32x16_bf16 v[18:33], v[230:233], v[244:247], v[18:33]
	v_sub_f32_e32 v169, v211, v168
	v_mul_f32_e32 v169, 0x3dd53b94, v169
	v_exp_f32_e32 v169, v169
	s_cmp_eq_u64 vcc, exec
	s_cselect_b64 s[18:19], -1, 0
	v_readfirstlane_b32 s4, v0
	s_nop 0
	s_cmp_lt_u32 s4, 0x100
	s_cbranch_scc1 .Lattn_e1_skip
	s_waitcnt vmcnt(0) lgkmcnt(0)
	s_barrier
.Lattn_e1_skip:
	v_cndmask_b32_e64 v172, v169, 1.0, s[18:19]
	v_cmp_gt_f32_e32 vcc, 1.0, v172
	s_cbranch_vccz .LBB0_1348
	s_and_saveexec_b64 s[4:5], s[0:1]
	ds_write_b32 v197, v172 offset:128
	s_or_b64 exec, exec, s[4:5]
	s_waitcnt lgkmcnt(0)
	v_add_u32_e32 v160, v196, v98
	ds_read_b128 v[148:151], v160 offset:224
	ds_read_b128 v[152:155], v160 offset:192
	ds_read_b128 v[156:159], v160 offset:160
	ds_read_b128 v[160:163], v160 offset:128
	v_mov_b32_e32 v228, 0xffffce00
	s_waitcnt lgkmcnt(3)
	v_pk_mul_f32 v[14:15], v[14:15], v[148:149]
	s_waitcnt lgkmcnt(2)
	v_pk_mul_f32 v[10:11], v[10:11], v[152:153]
	s_waitcnt lgkmcnt(1)
	v_pk_mul_f32 v[6:7], v[6:7], v[156:157]
	v_pk_mul_f32 v[16:17], v[16:17], v[150:151]
	v_pk_mul_f32 v[12:13], v[12:13], v[154:155]
	v_pk_mul_f32 v[8:9], v[8:9], v[158:159]
	s_waitcnt lgkmcnt(0)
	v_pk_mul_f32 v[4:5], v[4:5], v[162:163]
	v_pk_mul_f32 v[2:3], v[2:3], v[160:161]
	v_pk_mul_f32 v[62:63], v[62:63], v[148:149]
	v_pk_mul_f32 v[58:59], v[58:59], v[152:153]
	v_pk_mul_f32 v[54:55], v[54:55], v[156:157]
	v_pk_mul_f32 v[64:65], v[64:65], v[150:151]
	v_pk_mul_f32 v[60:61], v[60:61], v[154:155]
	v_pk_mul_f32 v[56:57], v[56:57], v[158:159]
	v_pk_mul_f32 v[52:53], v[52:53], v[162:163]
	v_pk_mul_f32 v[50:51], v[50:51], v[160:161]
	v_pk_mul_f32 v[46:47], v[46:47], v[148:149]
	v_pk_mul_f32 v[42:43], v[42:43], v[152:153]
	v_pk_mul_f32 v[38:39], v[38:39], v[156:157]
	v_pk_mul_f32 v[48:49], v[48:49], v[150:151]
	v_pk_mul_f32 v[44:45], v[44:45], v[154:155]
	v_pk_mul_f32 v[40:41], v[40:41], v[158:159]
	v_pk_mul_f32 v[36:37], v[36:37], v[162:163]
	v_pk_mul_f32 v[34:35], v[34:35], v[160:161]
	v_pk_mul_f32 v[30:31], v[30:31], v[148:149]
	v_pk_mul_f32 v[26:27], v[26:27], v[152:153]
	v_pk_mul_f32 v[22:23], v[22:23], v[156:157]
	v_pk_mul_f32 v[32:33], v[32:33], v[150:151]
	v_pk_mul_f32 v[28:29], v[28:29], v[154:155]
	v_pk_mul_f32 v[24:25], v[24:25], v[158:159]
	v_pk_mul_f32 v[20:21], v[20:21], v[162:163]
	v_pk_mul_f32 v[18:19], v[18:19], v[160:161]
	s_branch .LBB0_1349

.LBB0_1349:
	v_cndmask_b32_e64 v173, v168, v211, s[18:19]
	v_mul_f32_e32 v164, 0xbdd53b94, v173
	v_fmamk_f32 v82, v82, 0x3dd53b94, v164
	v_fmamk_f32 v83, v83, 0x3dd53b94, v164
	v_fmamk_f32 v84, v84, 0x3dd53b94, v164
	v_fmamk_f32 v85, v85, 0x3dd53b94, v164
	v_fmamk_f32 v86, v86, 0x3dd53b94, v164
	v_fmamk_f32 v87, v87, 0x3dd53b94, v164
	v_fmamk_f32 v88, v88, 0x3dd53b94, v164
	v_fmamk_f32 v89, v89, 0x3dd53b94, v164
	v_fmamk_f32 v90, v90, 0x3dd53b94, v164
	v_fmamk_f32 v91, v91, 0x3dd53b94, v164
	v_fmamk_f32 v92, v92, 0x3dd53b94, v164
	v_fmamk_f32 v93, v93, 0x3dd53b94, v164
	v_fmamk_f32 v94, v94, 0x3dd53b94, v164
	v_fmamk_f32 v95, v95, 0x3dd53b94, v164
	v_fmamk_f32 v96, v96, 0x3dd53b94, v164
	v_fmamk_f32 v97, v97, 0x3dd53b94, v164
	v_fmamk_f32 v229, v68, 0x3dd53b94, v164
	v_fmamk_f32 v230, v69, 0x3dd53b94, v164
	v_fmamk_f32 v168, v73, 0x3dd53b94, v164
	v_fmamk_f32 v169, v74, 0x3dd53b94, v164
	v_fmamk_f32 v175, v66, 0x3dd53b94, v164
	v_fmamk_f32 v211, v67, 0x3dd53b94, v164
	v_fmamk_f32 v231, v70, 0x3dd53b94, v164
	v_fmamk_f32 v166, v71, 0x3dd53b94, v164
	v_fmamk_f32 v167, v72, 0x3dd53b94, v164
	v_fmamk_f32 v170, v75, 0x3dd53b94, v164
	v_fmamk_f32 v171, v76, 0x3dd53b94, v164
	v_fmamk_f32 v174, v77, 0x3dd53b94, v164
	v_fmamk_f32 v165, v78, 0x3dd53b94, v164
	v_exp_f32_e32 v161, v82
	v_exp_f32_e32 v163, v83
	v_exp_f32_e32 v159, v84
	v_exp_f32_e32 v162, v85
	v_exp_f32_e32 v158, v86
	v_exp_f32_e32 v160, v87
	v_exp_f32_e32 v156, v88
	v_exp_f32_e32 v157, v89
	v_exp_f32_e32 v153, v90
	v_exp_f32_e32 v155, v91
	v_exp_f32_e32 v152, v92
	v_exp_f32_e32 v154, v93
	v_exp_f32_e32 v149, v94
	v_exp_f32_e32 v151, v95
	v_exp_f32_e32 v148, v96
	v_exp_f32_e32 v150, v97
	v_fmamk_f32 v232, v79, 0x3dd53b94, v164
	v_fmamk_f32 v233, v80, 0x3dd53b94, v164
	v_fmac_f32_e32 v164, 0x3dd53b94, v81
	v_readfirstlane_b32 s4, v0
	s_nop 0
	s_cmp_ge_u32 s4, 0x100
	s_cbranch_scc1 .Lattn_l1_skip
	s_waitcnt vmcnt(0) lgkmcnt(0)
	s_barrier
.Lattn_l1_skip:
	ds_read_b128 v[214:217], v203
	ds_read_b128 v[222:225], v203 offset:12288
	ds_read_b128 v[236:239], v204
	ds_read_b128 v[240:243], v204 offset:12288
	ds_read_b128 v[66:69], v201 offset:12288
	ds_read_b128 v[70:73], v201
	ds_read_b128 v[244:247], v202
	ds_read_b128 v[176:179], v202 offset:12288
	v_exp_f32_e32 v166, v166
	v_exp_f32_e32 v167, v167
	v_exp_f32_e32 v218, v169
	s_waitcnt lgkmcnt(2)
	v_mfma_f32_32x32x16_bf16 v[82:97], v[70:73], v[128:131], 0
	v_exp_f32_e32 v219, v170
	v_exp_f32_e32 v165, v165
	v_exp_f32_e32 v164, v164
	v_mfma_f32_32x32x16_bf16 v[82:97], v[214:217], v[124:127], v[82:97]
	v_mfma_f32_32x32x16_bf16 v[82:97], v[236:239], v[120:123], v[82:97]
	v_mfma_f32_32x32x16_bf16 v[66:81], v[66:69], v[128:131], 0
	s_waitcnt lgkmcnt(1)
	v_mfma_f32_32x32x16_bf16 v[82:97], v[244:247], v[116:119], v[82:97]
	v_mfma_f32_32x32x16_bf16 v[66:81], v[222:225], v[124:127], v[66:81]
	ds_read_b128 v[214:217], v201 offset:128
	ds_read_b128 v[222:225], v201 offset:12416
	s_waitcnt lgkmcnt(1)
	v_mfma_f32_32x32x16_bf16 v[82:97], v[214:217], v[112:115], v[82:97]
	v_mfma_f32_32x32x16_bf16 v[66:81], v[240:243], v[120:123], v[66:81]
	ds_read_b128 v[236:239], v203 offset:128
	ds_read_b128 v[240:243], v203 offset:12416
	s_waitcnt lgkmcnt(1)
	v_mfma_f32_32x32x16_bf16 v[82:97], v[236:239], v[108:111], v[82:97]
	v_mfma_f32_32x32x16_bf16 v[66:81], v[176:179], v[116:119], v[66:81]
	ds_read_b128 v[176:179], v204 offset:128
	ds_read_b128 v[244:247], v204 offset:12416
	s_waitcnt lgkmcnt(1)
	v_mfma_f32_32x32x16_bf16 v[82:97], v[176:179], v[104:107], v[82:97]
	v_mfma_f32_32x32x16_bf16 v[66:81], v[222:225], v[112:115], v[66:81]
	ds_read_b128 v[214:217], v202 offset:128
	ds_read_b128 v[222:225], v202 offset:12416
	s_waitcnt lgkmcnt(1)
	v_mfma_f32_32x32x16_bf16 v[82:97], v[214:217], v[100:103], v[82:97]
	v_mfma_f32_32x32x16_bf16 v[66:81], v[240:243], v[108:111], v[66:81]
	ds_read_b128 v[236:239], v201 offset:256
	ds_read_b128 v[240:243], v201 offset:12544
	s_waitcnt lgkmcnt(1)
	v_mfma_f32_32x32x16_bf16 v[82:97], v[236:239], v[144:147], v[82:97]
	v_mfma_f32_32x32x16_bf16 v[66:81], v[244:247], v[104:107], v[66:81]
	ds_read_b128 v[176:179], v203 offset:256
	ds_read_b128 v[244:247], v203 offset:12544
	s_waitcnt lgkmcnt(1)
	v_mfma_f32_32x32x16_bf16 v[82:97], v[176:179], v[140:143], v[82:97]
	v_exp_f32_e32 v178, v175
	v_exp_f32_e32 v179, v211
	v_exp_f32_e32 v211, v229
	v_mfma_f32_32x32x16_bf16 v[66:81], v[222:225], v[100:103], v[66:81]
	ds_read_b128 v[214:217], v204 offset:256
	ds_read_b128 v[222:225], v204 offset:12544
	s_waitcnt lgkmcnt(1)
	v_mfma_f32_32x32x16_bf16 v[82:97], v[214:217], v[136:139], v[82:97]
	v_exp_f32_e32 v217, v168
	v_add_f32_e32 v168, 0, v161
	v_add_f32_e32 v168, v163, v168
	v_add_f32_e32 v168, v159, v168
	v_add_f32_e32 v168, v162, v168
	v_add_f32_e32 v168, v158, v168
	v_add_f32_e32 v168, v160, v168
	v_mfma_f32_32x32x16_bf16 v[66:81], v[240:243], v[144:147], v[66:81]
	v_add_f32_e32 v168, v156, v168
	v_add_f32_e32 v168, v157, v168
	v_add_f32_e32 v168, v153, v168
	v_add_f32_e32 v168, v155, v168
	v_add_f32_e32 v168, v152, v168
	v_add_f32_e32 v168, v154, v168
	v_add_f32_e32 v168, v149, v168
	v_mfma_f32_32x32x16_bf16 v[66:81], v[244:247], v[140:143], v[66:81]
	v_add_f32_e32 v168, v151, v168
	v_add_f32_e32 v168, v148, v168
	v_exp_f32_e32 v215, v230
	v_add_f32_e32 v168, v150, v168
	v_exp_f32_e32 v216, v231
	v_add_f32_e32 v168, v178, v168
	v_add_f32_e32 v168, v179, v168
	s_waitcnt lgkmcnt(0)
	v_mfma_f32_32x32x16_bf16 v[66:81], v[222:225], v[136:139], v[66:81]
	v_add_f32_e32 v168, v211, v168
	v_add_f32_e32 v168, v215, v168
	v_add_f32_e32 v168, v216, v168
	ds_read_b128 v[236:239], v202 offset:256
	ds_read_b128 v[240:243], v202 offset:12544
	v_add_f32_e32 v168, v166, v168
	v_exp_f32_e32 v223, v171
	v_add_f32_e32 v168, v167, v168
	v_exp_f32_e32 v224, v174
	v_add_f32_e32 v168, v217, v168
	v_add_f32_e32 v168, v218, v168
	v_exp_f32_e32 v225, v232
	v_add_f32_e32 v168, v219, v168
	s_waitcnt lgkmcnt(1)
	v_mfma_f32_32x32x16_bf16 v[82:97], v[236:239], v[132:135], v[82:97]
	v_exp_f32_e32 v231, v233
	v_add_f32_e32 v168, v223, v168
	v_add_f32_e32 v168, v224, v168
	v_add_f32_e32 v168, v165, v168
	v_add_f32_e32 v168, v225, v168
	v_add_f32_e32 v168, v231, v168
	v_add_f32_e32 v229, v164, v168
	s_waitcnt lgkmcnt(0)
	v_mfma_f32_32x32x16_bf16 v[66:81], v[240:243], v[132:135], v[66:81]
	v_mov_b32_e32 v230, v229
	v_cvt_pk_bf16_f32 v168, v161, v163
	v_cvt_pk_bf16_f32 v169, v159, v162
	v_cvt_pk_bf16_f32 v170, v158, v160
	v_cvt_pk_bf16_f32 v171, v156, v157
	s_nop 1
	v_permlane32_swap_b32_e32 v229, v230
	v_permlane32_swap_b32_e32 v168, v170
	v_permlane32_swap_b32_e32 v169, v171
	v_cvt_pk_bf16_f32 v174, v153, v155
	v_cvt_pk_bf16_f32 v175, v152, v154
	v_cvt_pk_bf16_f32 v176, v149, v151
	v_cvt_pk_bf16_f32 v177, v148, v150
	v_cvt_pk_bf16_f32 v214, v178, v179
	v_cvt_pk_bf16_f32 v215, v211, v215
	v_cvt_pk_bf16_f32 v216, v216, v166
	v_cvt_pk_bf16_f32 v217, v167, v217
	v_cvt_pk_bf16_f32 v222, v218, v219
	v_cvt_pk_bf16_f32 v223, v223, v224
	v_cvt_pk_bf16_f32 v224, v165, v225
	v_cvt_pk_bf16_f32 v225, v231, v164
	s_nop 0
	v_permlane32_swap_b32_e32 v174, v176
	v_permlane32_swap_b32_e32 v175, v177
	v_permlane32_swap_b32_e32 v214, v216
	v_permlane32_swap_b32_e32 v215, v217
	v_permlane32_swap_b32_e32 v222, v224
	v_permlane32_swap_b32_e32 v223, v225
	v_readfirstlane_b32 s4, v0
	s_nop 0
	s_lshl_b32 s5, s4, 4
	s_mul_i32 s4, s5, 3
	s_add_i32 m0, s4, 0xe000
	s_nop 0
	global_load_lds_dwordx4 v[182:183], off
	s_add_i32 m0, s4, 0xe400
	s_nop 0
	global_load_lds_dwordx4 v[184:185], off
	s_add_i32 m0, s4, 0xe800
	s_nop 0
	global_load_lds_dwordx4 v[186:187], off
	s_lshl_b32 s5, s5, 1
	s_mov_b32 m0, s5
	s_nop 0
	global_load_lds_dwordx4 v[206:207], off
	s_add_i32 m0, s5, 0x380
	s_nop 0
	global_load_lds_dwordx4 v[206:207], off offset:128
	v_add_co_u32_e32 v182, vcc, v182, v205
	s_nop 1
	v_addc_co_u32_e32 v183, vcc, 0, v183, vcc
	v_add_co_u32_e32 v184, vcc, v184, v208
	s_nop 1
	v_addc_co_u32_e32 v185, vcc, 0, v185, vcc
	v_add_co_u32_e32 v186, vcc, v186, v209
	s_nop 1
	v_addc_co_u32_e32 v187, vcc, 0, v187, vcc
	v_add_co_u32_e32 v206, vcc, 0x38000, v206
	s_nop 1
	v_addc_co_u32_e32 v207, vcc, 0, v207, vcc
	ds_read_b64_tr_b16 v[188:189], v198 offset:0
	ds_read_b64_tr_b16 v[190:191], v198 offset:0x800
	ds_read_b64_tr_b16 v[236:237], v198 offset:0x1000
	ds_read_b64_tr_b16 v[238:239], v198 offset:0x1800
	ds_read_b64_tr_b16 v[240:241], v198 offset:0x2000
	ds_read_b64_tr_b16 v[242:243], v198 offset:0x2800
	ds_read_b64_tr_b16 v[244:245], v198 offset:0x3000
	ds_read_b64_tr_b16 v[246:247], v198 offset:0x3800
	s_waitcnt lgkmcnt(0)
	s_nop 0
	v_mfma_f32_32x32x16_bf16 v[2:17], v[168:171], v[188:191], v[2:17]
	ds_read_b64_tr_b16 v[188:189], v198 offset:0x200
	ds_read_b64_tr_b16 v[190:191], v198 offset:0xa00
	v_mfma_f32_32x32x16_bf16 v[2:17], v[174:177], v[236:239], v[2:17]
	ds_read_b64_tr_b16 v[236:237], v198 offset:0x1200
	ds_read_b64_tr_b16 v[238:239], v198 offset:0x1a00
	v_mfma_f32_32x32x16_bf16 v[2:17], v[214:217], v[240:243], v[2:17]
	ds_read_b64_tr_b16 v[240:241], v198 offset:0x2200
	ds_read_b64_tr_b16 v[242:243], v198 offset:0x2a00
	v_mfma_f32_32x32x16_bf16 v[2:17], v[222:225], v[244:247], v[2:17]
	ds_read_b64_tr_b16 v[244:245], v198 offset:0x3200
	ds_read_b64_tr_b16 v[246:247], v198 offset:0x3a00
	s_waitcnt lgkmcnt(0)
	v_mfma_f32_32x32x16_bf16 v[50:65], v[168:171], v[188:191], v[50:65]
	ds_read_b64_tr_b16 v[188:189], v198 offset:0x400
	ds_read_b64_tr_b16 v[190:191], v198 offset:0xc00
	v_mfma_f32_32x32x16_bf16 v[50:65], v[174:177], v[236:239], v[50:65]
	ds_read_b64_tr_b16 v[236:237], v198 offset:0x1400
	ds_read_b64_tr_b16 v[238:239], v198 offset:0x1c00
	v_mfma_f32_32x32x16_bf16 v[50:65], v[214:217], v[240:243], v[50:65]
	ds_read_b64_tr_b16 v[240:241], v198 offset:0x2400
	ds_read_b64_tr_b16 v[242:243], v198 offset:0x2c00
	v_mfma_f32_32x32x16_bf16 v[50:65], v[222:225], v[244:247], v[50:65]
	ds_read_b64_tr_b16 v[244:245], v198 offset:0x3400
	ds_read_b64_tr_b16 v[246:247], v198 offset:0x3c00
	s_waitcnt lgkmcnt(0)
	v_mfma_f32_32x32x16_bf16 v[34:49], v[168:171], v[188:191], v[34:49]
	ds_read_b64_tr_b16 v[188:189], v198 offset:0x600
	ds_read_b64_tr_b16 v[190:191], v198 offset:0xe00
	v_mfma_f32_32x32x16_bf16 v[34:49], v[174:177], v[236:239], v[34:49]
	ds_read_b64_tr_b16 v[236:237], v198 offset:0x1600
	ds_read_b64_tr_b16 v[238:239], v198 offset:0x1e00
	v_mfma_f32_32x32x16_bf16 v[34:49], v[214:217], v[240:243], v[34:49]
	ds_read_b64_tr_b16 v[240:241], v198 offset:0x2600
	ds_read_b64_tr_b16 v[242:243], v198 offset:0x2e00
	v_mfma_f32_32x32x16_bf16 v[34:49], v[222:225], v[244:247], v[34:49]
	ds_read_b64_tr_b16 v[244:245], v198 offset:0x3600
	ds_read_b64_tr_b16 v[246:247], v198 offset:0x3e00
	s_waitcnt lgkmcnt(0)
	v_mfma_f32_32x32x16_bf16 v[18:33], v[168:171], v[188:191], v[18:33]
	v_max_f32_e32 v168, v83, v83
	v_max_f32_e32 v169, v82, v82
	v_max_f32_e32 v168, v169, v168
	v_max3_f32 v168, v168, v84, v85
	v_max3_f32 v168, v168, v86, v87
	v_max3_f32 v168, v168, v88, v89
	v_max3_f32 v168, v168, v90, v91
	v_max3_f32 v168, v168, v92, v93
	v_max3_f32 v168, v168, v94, v95
	v_mfma_f32_32x32x16_bf16 v[18:33], v[174:177], v[236:239], v[18:33]
	v_max3_f32 v168, v168, v96, v97
	v_max3_f32 v168, v168, v66, v67
	v_max3_f32 v168, v168, v68, v69
	v_max3_f32 v168, v168, v70, v71
	v_max3_f32 v168, v168, v72, v73
	v_max3_f32 v168, v168, v74, v75
	v_max3_f32 v168, v168, v76, v77
	v_max3_f32 v168, v168, v78, v79
	v_mfma_f32_32x32x16_bf16 v[18:33], v[214:217], v[240:243], v[18:33]
	v_max3_f32 v168, v168, v80, v81
	v_mov_b32_e32 v169, v168
	s_nop 1
	v_permlane32_swap_b32_e32 v168, v169
	v_max_f32_e32 v169, v169, v169
	v_max_f32_e32 v168, v168, v168
	v_max_f32_e32 v168, v168, v169
	v_sub_f32_e32 v169, v168, v173
	v_cmp_ge_f32_e32 vcc, s11, v169
	v_max_f32_e32 v169, v173, v173
	v_max_f32_e32 v169, v169, v168
	v_mfma_f32_32x32x16_bf16 v[18:33], v[222:225], v[244:247], v[18:33]
	v_sub_f32_e32 v168, v173, v169
	v_mul_f32_e32 v168, 0x3dd53b94, v168
	v_exp_f32_e32 v168, v168
	s_cmp_eq_u64 vcc, exec
	s_cselect_b64 s[18:19], -1, 0
	v_readfirstlane_b32 s4, v0
	s_nop 0
	s_cmp_lt_u32 s4, 0x100
	s_cbranch_scc1 .Lattn_e2_skip
	s_waitcnt vmcnt(0) lgkmcnt(0)
	s_barrier
.Lattn_e2_skip:
	v_cndmask_b32_e64 v168, v168, 1.0, s[18:19]
	v_cmp_gt_f32_e32 vcc, 1.0, v168
	s_cbranch_vccz .LBB0_1353
	s_mov_b64 s[4:5], exec
	s_and_b64 s[22:23], s[4:5], s[0:1]
	v_mov_b32_e32 v246, v227
	s_mov_b64 exec, s[22:23]
	ds_write_b32 v197, v168 offset:128
	s_or_b64 exec, exec, s[4:5]
	s_waitcnt lgkmcnt(0)
	v_add_u32_e32 v160, v196, v98
	ds_read_b128 v[148:151], v160 offset:224
	ds_read_b128 v[152:155], v160 offset:192
	ds_read_b128 v[156:159], v160 offset:160
	ds_read_b128 v[160:163], v160 offset:128
	s_waitcnt lgkmcnt(3)
	v_pk_mul_f32 v[14:15], v[14:15], v[148:149]
	s_waitcnt lgkmcnt(2)
	v_pk_mul_f32 v[10:11], v[10:11], v[152:153]
	s_waitcnt lgkmcnt(1)
	v_pk_mul_f32 v[6:7], v[6:7], v[156:157]
	v_pk_mul_f32 v[16:17], v[16:17], v[150:151]
	v_pk_mul_f32 v[12:13], v[12:13], v[154:155]
	v_pk_mul_f32 v[8:9], v[8:9], v[158:159]
	s_waitcnt lgkmcnt(0)
	v_pk_mul_f32 v[4:5], v[4:5], v[162:163]
	v_pk_mul_f32 v[2:3], v[2:3], v[160:161]
	v_pk_mul_f32 v[62:63], v[62:63], v[148:149]
	v_pk_mul_f32 v[58:59], v[58:59], v[152:153]
	v_pk_mul_f32 v[54:55], v[54:55], v[156:157]
	v_pk_mul_f32 v[64:65], v[64:65], v[150:151]
	v_pk_mul_f32 v[60:61], v[60:61], v[154:155]
	v_pk_mul_f32 v[56:57], v[56:57], v[158:159]
	v_pk_mul_f32 v[52:53], v[52:53], v[162:163]
	v_pk_mul_f32 v[50:51], v[50:51], v[160:161]
	v_pk_mul_f32 v[46:47], v[46:47], v[148:149]
	v_pk_mul_f32 v[42:43], v[42:43], v[152:153]
	v_pk_mul_f32 v[38:39], v[38:39], v[156:157]
	v_pk_mul_f32 v[48:49], v[48:49], v[150:151]
	v_pk_mul_f32 v[44:45], v[44:45], v[154:155]
	v_pk_mul_f32 v[40:41], v[40:41], v[158:159]
	v_pk_mul_f32 v[36:37], v[36:37], v[162:163]
	v_pk_mul_f32 v[34:35], v[34:35], v[160:161]
	v_pk_mul_f32 v[30:31], v[30:31], v[148:149]
	v_pk_mul_f32 v[26:27], v[26:27], v[152:153]
	v_pk_mul_f32 v[22:23], v[22:23], v[156:157]
	v_pk_mul_f32 v[32:33], v[32:33], v[150:151]
	v_pk_mul_f32 v[28:29], v[28:29], v[154:155]
	v_pk_mul_f32 v[24:25], v[24:25], v[158:159]
	v_pk_mul_f32 v[20:21], v[20:21], v[162:163]
	v_pk_mul_f32 v[18:19], v[18:19], v[160:161]
	s_branch .LBB0_1354

.LBB0_1354:
	v_cndmask_b32_e64 v211, v169, v173, s[18:19]
	v_mul_f32_e32 v148, 0xbdd53b94, v211
	v_mov_b32_e32 v149, v148
	v_fmamk_f32 v82, v82, 0x3dd53b94, v148
	v_fmamk_f32 v83, v83, 0x3dd53b94, v148
	v_fmamk_f32 v84, v84, 0x3dd53b94, v148
	v_fmamk_f32 v85, v85, 0x3dd53b94, v148
	v_fmamk_f32 v86, v86, 0x3dd53b94, v148
	v_fmamk_f32 v87, v87, 0x3dd53b94, v148
	v_fmamk_f32 v88, v88, 0x3dd53b94, v148
	v_fmamk_f32 v89, v89, 0x3dd53b94, v148
	v_fmamk_f32 v90, v90, 0x3dd53b94, v148
	v_fmamk_f32 v91, v91, 0x3dd53b94, v148
	v_fmamk_f32 v92, v92, 0x3dd53b94, v148
	v_fmamk_f32 v93, v93, 0x3dd53b94, v148
	v_fmamk_f32 v94, v94, 0x3dd53b94, v148
	v_fmamk_f32 v95, v95, 0x3dd53b94, v148
	v_fmamk_f32 v96, v96, 0x3dd53b94, v148
	v_fmac_f32_e32 v149, 0x3dd53b94, v97
	v_exp_f32_e32 v169, v82
	v_exp_f32_e32 v191, v83
	v_exp_f32_e32 v170, v84
	v_exp_f32_e32 v192, v85
	v_exp_f32_e32 v190, v86
	v_exp_f32_e32 v193, v87
	v_exp_f32_e32 v171, v88
	v_exp_f32_e32 v189, v89
	v_exp_f32_e32 v173, v90
	v_exp_f32_e32 v175, v91
	v_exp_f32_e32 v174, v92
	v_exp_f32_e32 v188, v93
	v_exp_f32_e32 v164, v94
	v_exp_f32_e32 v166, v95
	v_exp_f32_e32 v165, v96
	v_exp_f32_e32 v167, v149
	v_pk_fma_f32 v[162:163], v[66:67], s[56:57], v[148:149] op_sel_hi:[1,0,0]
	v_add_f32_e32 v66, v212, v213
	v_fmac_f32_e32 v66, v210, v199
	v_add_f32_e32 v199, v229, v230
	s_add_i32 s8, s8, 2
	v_pk_fma_f32 v[160:161], v[68:69], s[56:57], v[148:149] op_sel_hi:[1,0,0]
	v_pk_fma_f32 v[156:157], v[70:71], s[56:57], v[148:149] op_sel_hi:[1,0,0]
	v_pk_fma_f32 v[152:153], v[72:73], s[56:57], v[148:149] op_sel_hi:[1,0,0]
	v_pk_fma_f32 v[150:151], v[74:75], s[56:57], v[148:149] op_sel_hi:[1,0,0]
	v_pk_fma_f32 v[158:159], v[76:77], s[56:57], v[148:149] op_sel_hi:[1,0,0]
	v_pk_fma_f32 v[154:155], v[78:79], s[56:57], v[148:149] op_sel_hi:[1,0,0]
	v_pk_fma_f32 v[148:149], v[80:81], s[56:57], v[148:149] op_sel_hi:[1,0,0]
	v_fmac_f32_e32 v199, v66, v172
	v_readfirstlane_b32 s4, v0
	s_nop 0
	s_cmp_ge_u32 s4, 0x100
	s_cbranch_scc1 .Lattn_l2_skip
	s_waitcnt vmcnt(0) lgkmcnt(0)
	s_barrier
.Lattn_l2_skip:
	s_cmp_ge_u32 s8, s3
	s_cbranch_scc1 .LBB0_1356
	v_mov_b32_e32 v227, 0x3200
	v_mov_b32_e32 v210, v168
	s_branch .LBB0_1344
